# sel tile: rescale test is one compare of the biased row max against a persistent threshold (the true max is formed only on the rescale path)
# speedup vs baseline: 1.0062x; 1.0062x over previous
; #define GAS __attribute__((address_space(1)))
; __device__ __forceinline__ unsigned pk4_fp8(float a, float b, float c, float d) { unsigned w = 0u; w = __builtin_amdgcn_cvt_pk_fp8_f32(a, b, w, false); w = __builtin_amdgcn_cvt_pk_fp8_f32(c, d, w, true); return w; }
; __device__ __forceinline__ void gs8_init(GS8& g, const bf16* qrow32) {
; #pragma unroll
;     for (int i = 0; i < 4; ++i) { const u32x4 w = *(const GAS u32x4*)(qrow32 + 8 * i);
;         g.q8[2 * i] = (int)pk4_fp8(bf_lo(w.x) * 8.f, bf_hi(w.x) * 8.f, bf_lo(w.y) * 8.f, bf_hi(w.y) * 8.f); g.q8[2 * i + 1] = (int)pk4_fp8(bf_lo(w.z) * 8.f, bf_hi(w.z) * 8.f, bf_lo(w.w) * 8.f, bf_hi(w.w) * 8.f); }
; #pragma unroll
;     for (int dt = 0; dt < 8; ++dt) g.o[dt] = (f32x4){0.f, 0.f, 0.f, 0.f};
;     g.m = -1e30f; g.l = 0.f;
; }
; template <bool DUMMY> __device__ __forceinline__ void sel_phase(Frame& F) {
;     ...
;     for (int unit = F.vcu; unit < 2048; unit += F.G, ++it) {
;         const int bh = unit >> 8, tl = unit & 255, tile = (it & 1) ? 255 - tl : tl, b = bh >> 2, kvh = bh & 3, t0 = tile * 64, cur = tile;
;         const int tokA = t0 + 8 * F.wave + (c >> 2), head = kvh * GQ + (c & 3);
;         const size_t qoff = ((size_t)(b * NH + head) * SEQ + tokA) * HD;
;         GS8 g0, g1; gs8_init(g0, Q + qoff + 32 * kq); gs8_init(g1, Q + qoff + 4 * HD + 32 * kq);
.LBB0_1782:
	s_cmp_lt_i32 s36, 1
	s_cbranch_scc1 .LBB0_1701
	s_waitcnt vmcnt(0)
	v_lshlrev_b32_e32 v34, 16, v0
	v_and_b32_e32 v0, 0xffff0000, v0
	v_mul_f32_e32 v34, 0x41000000, v34
	v_mul_f32_e32 v35, 0x41000000, v0
	v_mov_b32_e32 v0, v17
	v_cvt_pk_fp8_f32 v0, v34, v35
	v_lshlrev_b32_e32 v36, 16, v1
	v_and_b32_e32 v1, 0xffff0000, v1
	v_mul_f32_e32 v34, 0x41000000, v36
	v_mul_f32_e32 v1, 0x41000000, v1
	v_cvt_pk_fp8_f32 v0, v34, v1 op_sel:[0,0,1]
	v_lshlrev_b32_e32 v1, 16, v2
	v_mul_f32_e32 v34, 0x41000000, v1
	v_and_b32_e32 v1, 0xffff0000, v2
	v_mul_f32_e32 v2, 0x41000000, v1
	v_mov_b32_e32 v1, v17
	v_cvt_pk_fp8_f32 v1, v34, v2
	v_lshlrev_b32_e32 v35, 16, v3
	v_and_b32_e32 v3, 0xffff0000, v3
	v_mul_f32_e32 v2, 0x41000000, v35
	v_mul_f32_e32 v3, 0x41000000, v3
	v_cvt_pk_fp8_f32 v1, v2, v3 op_sel:[0,0,1]
	v_lshlrev_b32_e32 v2, 16, v30
	v_mul_f32_e32 v3, 0x41000000, v2
	v_and_b32_e32 v2, 0xffff0000, v30
	v_mul_f32_e32 v30, 0x41000000, v2
	v_mov_b32_e32 v2, v17
	v_cvt_pk_fp8_f32 v2, v3, v30
	v_lshlrev_b32_e32 v34, 16, v31
	v_and_b32_e32 v30, 0xffff0000, v31
	v_mul_f32_e32 v3, 0x41000000, v34
	v_mul_f32_e32 v30, 0x41000000, v30
	v_cvt_pk_fp8_f32 v2, v3, v30 op_sel:[0,0,1]
	v_lshlrev_b32_e32 v3, 16, v32
	v_mul_f32_e32 v30, 0x41000000, v3
	v_and_b32_e32 v3, 0xffff0000, v32
	v_mul_f32_e32 v31, 0x41000000, v3
	v_mov_b32_e32 v3, v17
	v_cvt_pk_fp8_f32 v3, v30, v31
	v_lshlrev_b32_e32 v32, 16, v33
	v_and_b32_e32 v31, 0xffff0000, v33
	v_mul_f32_e32 v30, 0x41000000, v32
	v_mul_f32_e32 v31, 0x41000000, v31
	v_cvt_pk_fp8_f32 v3, v30, v31 op_sel:[0,0,1]
	v_lshlrev_b32_e32 v30, 16, v4
	v_and_b32_e32 v4, 0xffff0000, v4
	v_mul_f32_e32 v30, 0x41000000, v30
	v_mul_f32_e32 v31, 0x41000000, v4
	v_mov_b32_e32 v4, v17
	v_cvt_pk_fp8_f32 v4, v30, v31
	v_lshlrev_b32_e32 v32, 16, v5
	v_and_b32_e32 v5, 0xffff0000, v5
	v_mul_f32_e32 v30, 0x41000000, v32
	v_mul_f32_e32 v5, 0x41000000, v5
	v_cvt_pk_fp8_f32 v4, v30, v5 op_sel:[0,0,1]
	v_lshlrev_b32_e32 v5, 16, v6
	v_mul_f32_e32 v30, 0x41000000, v5
	v_and_b32_e32 v5, 0xffff0000, v6
	v_mul_f32_e32 v6, 0x41000000, v5
	v_mov_b32_e32 v5, v17
	v_cvt_pk_fp8_f32 v5, v30, v6
	v_lshlrev_b32_e32 v31, 16, v7
	v_and_b32_e32 v7, 0xffff0000, v7
	v_mul_f32_e32 v6, 0x41000000, v31
	v_mul_f32_e32 v7, 0x41000000, v7
	v_cvt_pk_fp8_f32 v5, v6, v7 op_sel:[0,0,1]
	v_lshlrev_b32_e32 v6, 16, v26
	v_mul_f32_e32 v7, 0x41000000, v6
	v_and_b32_e32 v6, 0xffff0000, v26
	v_mul_f32_e32 v26, 0x41000000, v6
	v_mov_b32_e32 v6, v17
	v_cvt_pk_fp8_f32 v6, v7, v26
	v_lshlrev_b32_e32 v30, 16, v27
	v_and_b32_e32 v26, 0xffff0000, v27
	v_mul_f32_e32 v7, 0x41000000, v30
	v_mul_f32_e32 v26, 0x41000000, v26
	v_cvt_pk_fp8_f32 v6, v7, v26 op_sel:[0,0,1]
	v_lshlrev_b32_e32 v7, 16, v28
	v_mul_f32_e32 v26, 0x41000000, v7
	v_and_b32_e32 v7, 0xffff0000, v28
	v_mul_f32_e32 v27, 0x41000000, v7
	v_mov_b32_e32 v7, v17
	v_cvt_pk_fp8_f32 v7, v26, v27
	v_lshlrev_b32_e32 v28, 16, v29
	v_and_b32_e32 v27, 0xffff0000, v29
	v_mul_f32_e32 v26, 0x41000000, v28
	v_mul_f32_e32 v27, 0x41000000, v27
	v_cvt_pk_fp8_f32 v7, v26, v27 op_sel:[0,0,1]
	v_lshlrev_b32_e32 v26, 16, v8
	v_and_b32_e32 v8, 0xffff0000, v8
	v_mul_f32_e32 v26, 0x41000000, v26
	v_mul_f32_e32 v27, 0x41000000, v8
	v_mov_b32_e32 v8, v17
	v_cvt_pk_fp8_f32 v8, v26, v27
	v_lshlrev_b32_e32 v28, 16, v9
	v_and_b32_e32 v9, 0xffff0000, v9
	v_mul_f32_e32 v26, 0x41000000, v28
	v_mul_f32_e32 v9, 0x41000000, v9
	v_cvt_pk_fp8_f32 v8, v26, v9 op_sel:[0,0,1]
	v_lshlrev_b32_e32 v9, 16, v10
	v_mul_f32_e32 v26, 0x41000000, v9
	v_and_b32_e32 v9, 0xffff0000, v10
	v_mul_f32_e32 v10, 0x41000000, v9
	v_mov_b32_e32 v9, v17
	v_cvt_pk_fp8_f32 v9, v26, v10
	v_lshlrev_b32_e32 v27, 16, v11
	v_and_b32_e32 v11, 0xffff0000, v11
	v_mul_f32_e32 v10, 0x41000000, v27
	v_mul_f32_e32 v11, 0x41000000, v11
	v_cvt_pk_fp8_f32 v9, v10, v11 op_sel:[0,0,1]
	v_lshlrev_b32_e32 v10, 16, v22
	v_mul_f32_e32 v11, 0x41000000, v10
	v_and_b32_e32 v10, 0xffff0000, v22
	v_mul_f32_e32 v22, 0x41000000, v10
	v_mov_b32_e32 v10, v17
	v_cvt_pk_fp8_f32 v10, v11, v22
	v_lshlrev_b32_e32 v26, 16, v23
	v_and_b32_e32 v22, 0xffff0000, v23
	v_mul_f32_e32 v11, 0x41000000, v26
	v_mul_f32_e32 v22, 0x41000000, v22
	v_cvt_pk_fp8_f32 v10, v11, v22 op_sel:[0,0,1]
	v_lshlrev_b32_e32 v11, 16, v24
	v_mul_f32_e32 v22, 0x41000000, v11
	v_and_b32_e32 v11, 0xffff0000, v24
	v_mul_f32_e32 v23, 0x41000000, v11
; #define GAS __attribute__((address_space(1)))
; __device__ __forceinline__ unsigned pk4_fp8(float a, float b, float c, float d) { unsigned w = 0u; w = __builtin_amdgcn_cvt_pk_fp8_f32(a, b, w, false); w = __builtin_amdgcn_cvt_pk_fp8_f32(c, d, w, true); return w; }
; __device__ __forceinline__ void gs8_init(GS8& g, const bf16* qrow32) {
; #pragma unroll
;     for (int i = 0; i < 4; ++i) { const u32x4 w = *(const GAS u32x4*)(qrow32 + 8 * i);
;         g.q8[2 * i] = (int)pk4_fp8(bf_lo(w.x) * 8.f, bf_hi(w.x) * 8.f, bf_lo(w.y) * 8.f, bf_hi(w.y) * 8.f); g.q8[2 * i + 1] = (int)pk4_fp8(bf_lo(w.z) * 8.f, bf_hi(w.z) * 8.f, bf_lo(w.w) * 8.f, bf_hi(w.w) * 8.f); }
; #pragma unroll
;     for (int dt = 0; dt < 8; ++dt) g.o[dt] = (f32x4){0.f, 0.f, 0.f, 0.f};
;     g.m = -1e30f; g.l = 0.f;
; }
; template <bool DUMMY> __device__ __forceinline__ void sel_phase(Frame& F) {
;     ...
;         u32x2 dcur = PD[F.wave]; unsigned cj = (unsigned)__builtin_amdgcn_readfirstlane((int)dcur.x), cb = (unsigned)__builtin_amdgcn_readfirstlane((int)dcur.y);
;     ...
;         SEL_DMA3(cj, F.lds);
	v_mov_b32_e32 v11, v17
	v_cvt_pk_fp8_f32 v11, v22, v23
	v_lshlrev_b32_e32 v24, 16, v25
	v_and_b32_e32 v23, 0xffff0000, v25
	v_mul_f32_e32 v22, 0x41000000, v24
	v_mul_f32_e32 v23, 0x41000000, v23
	v_cvt_pk_fp8_f32 v11, v22, v23 op_sel:[0,0,1]
	v_lshlrev_b32_e32 v22, 16, v12
	v_and_b32_e32 v12, 0xffff0000, v12
	v_mul_f32_e32 v22, 0x41000000, v22
	v_mul_f32_e32 v23, 0x41000000, v12
	v_mov_b32_e32 v12, v17
	v_cvt_pk_fp8_f32 v12, v22, v23
	v_lshlrev_b32_e32 v24, 16, v13
	v_and_b32_e32 v13, 0xffff0000, v13
	v_mul_f32_e32 v22, 0x41000000, v24
	v_mul_f32_e32 v13, 0x41000000, v13
	v_cvt_pk_fp8_f32 v12, v22, v13 op_sel:[0,0,1]
	v_lshlrev_b32_e32 v13, 16, v14
	v_mul_f32_e32 v22, 0x41000000, v13
	v_and_b32_e32 v13, 0xffff0000, v14
	v_mul_f32_e32 v14, 0x41000000, v13
	v_mov_b32_e32 v13, v17
	v_cvt_pk_fp8_f32 v13, v22, v14
	v_lshlrev_b32_e32 v23, 16, v15
	v_and_b32_e32 v15, 0xffff0000, v15
	v_mul_f32_e32 v14, 0x41000000, v23
	v_mul_f32_e32 v15, 0x41000000, v15
	v_cvt_pk_fp8_f32 v13, v14, v15 op_sel:[0,0,1]
	v_lshlrev_b32_e32 v14, 16, v18
	v_mul_f32_e32 v15, 0x41000000, v14
	v_and_b32_e32 v14, 0xffff0000, v18
	v_mul_f32_e32 v18, 0x41000000, v14
	v_mov_b32_e32 v14, v17
	v_cvt_pk_fp8_f32 v14, v15, v18
	v_lshlrev_b32_e32 v22, 16, v19
	v_and_b32_e32 v18, 0xffff0000, v19
	v_mul_f32_e32 v15, 0x41000000, v22
	v_mul_f32_e32 v18, 0x41000000, v18
	v_cvt_pk_fp8_f32 v14, v15, v18 op_sel:[0,0,1]
	v_lshlrev_b32_e32 v15, 16, v20
	v_mul_f32_e32 v18, 0x41000000, v15
	v_and_b32_e32 v15, 0xffff0000, v20
	v_mul_f32_e32 v19, 0x41000000, v15
	v_mov_b32_e32 v15, v17
	v_cvt_pk_fp8_f32 v15, v18, v19
	v_lshlrev_b32_e32 v20, 16, v21
	v_and_b32_e32 v19, 0xffff0000, v21
	v_mul_f32_e32 v18, 0x41000000, v20
	v_mul_f32_e32 v19, 0x41000000, v19
	v_cvt_pk_fp8_f32 v15, v18, v19 op_sel:[0,0,1]
	v_mov_b32_e32 v52, v17
	v_mov_b32_e32 v53, v17
	v_mov_b32_e32 v54, v17
	v_mov_b32_e32 v55, v17
	v_mov_b64_e32 v[58:59], v[54:55]
	v_mov_b64_e32 v[62:63], v[54:55]
	v_mov_b64_e32 v[66:67], v[54:55]
	v_mov_b64_e32 v[70:71], v[54:55]
	v_mov_b64_e32 v[74:75], v[54:55]
	v_mov_b64_e32 v[78:79], v[54:55]
	v_mov_b64_e32 v[82:83], v[54:55]
	v_mov_b64_e32 v[20:21], v[52:53]
	v_mov_b64_e32 v[24:25], v[52:53]
	v_mov_b64_e32 v[28:29], v[52:53]
	v_mov_b64_e32 v[32:33], v[52:53]
	v_mov_b64_e32 v[36:37], v[52:53]
	v_mov_b64_e32 v[40:41], v[52:53]
	v_mov_b64_e32 v[44:45], v[52:53]
	v_mov_b64_e32 v[48:49], v[52:53]
	v_add_u32_e32 v184, -2, v16
	v_add_u32_e32 v185, -3, v16
	s_add_i32 s68, s55, -16
	v_subrev_u32_e32 v186, 17, v16
	v_subrev_u32_e32 v187, 18, v16
	v_subrev_u32_e32 v188, 19, v16
	s_sub_i32 s69, s55, 32
	v_subrev_u32_e32 v189, 33, v16
	v_subrev_u32_e32 v190, 34, v16
	v_subrev_u32_e32 v191, 35, v16
	s_sub_i32 s70, s55, 48
	v_subrev_u32_e32 v192, 49, v16
	v_subrev_u32_e32 v193, 50, v16
	v_subrev_u32_e32 v194, 51, v16
	v_or_b32_e32 v195, 4, v16
	v_add_u32_e32 v196, 2, v16
	v_add_u32_e32 v197, 1, v16
	s_add_i32 s71, s55, -12
	v_add_u32_e32 v198, -13, v16
	v_add_u32_e32 v199, -14, v16
	v_add_u32_e32 v200, -15, v16
	s_sub_i32 s72, s55, 28
	v_subrev_u32_e32 v201, 29, v16
	v_subrev_u32_e32 v202, 30, v16
	v_subrev_u32_e32 v203, 31, v16
	s_sub_i32 s73, s55, 44
	v_subrev_u32_e32 v204, 45, v16
	v_subrev_u32_e32 v205, 46, v16
	v_subrev_u32_e32 v206, 47, v16
	s_max_i32 s89, s59, 1
	s_mov_b32 s36, 0
	s_add_i32 s37, s84, 64
	v_mov_b32_e32 v224, s37
	ds_read_b64 v[224:225], v224
	v_mov_b32_e32 v19, 0xf149f2ca
	v_mov_b32_e32 v183, 0
	v_mov_b64_e32 v[56:57], v[52:53]
	v_mov_b64_e32 v[60:61], v[52:53]
	v_mov_b64_e32 v[64:65], v[52:53]
	v_mov_b64_e32 v[68:69], v[52:53]
	v_mov_b64_e32 v[72:73], v[52:53]
	v_mov_b64_e32 v[76:77], v[52:53]
	v_mov_b64_e32 v[80:81], v[52:53]
	v_mov_b32_e32 v182, 0
	v_mov_b32_e32 v117, 0xf149f2ca
	v_mov_b32_e32 v216, 0x40a00000
	v_mov_b32_e32 v217, 0xc0a00000
	v_mov_b32_e32 v218, 0xf149f2ca
	v_mov_b32_e32 v226, 0xf149f2ca
	v_mov_b32_e32 v227, 0xf149f2ca
	v_mov_b32_e32 v219, 0
	v_mov_b32_e32 v220, 0x40a00000
	v_mov_b32_e32 v221, 0xc0a00000
	v_mov_b32_e32 v222, 0xf149f2ca
	v_mov_b32_e32 v223, 0
	v_mov_b64_e32 v[22:23], v[54:55]
	v_mov_b64_e32 v[26:27], v[54:55]
	v_mov_b64_e32 v[30:31], v[54:55]
	v_mov_b64_e32 v[34:35], v[54:55]
	v_mov_b64_e32 v[38:39], v[54:55]
	v_mov_b64_e32 v[42:43], v[54:55]
	v_mov_b64_e32 v[46:47], v[54:55]
	v_mov_b64_e32 v[50:51], v[54:55]

; template <class G> __device__ __forceinline__ void online_sm8(f32x4 (&s)[4], G& g, const float ref) {
;     float mx = s[0][0];
; #pragma unroll
;     for (int T_ = 0; T_ < 4; ++T_)
; #pragma unroll
;         for (int i = 0; i < 4; ++i) mx = fmaxf(mx, s[T_][i]);
;     const float t = mx + (ref - 5.f);
;     if (!__all(t <= g.m + SM_THR8)) {
.LBB0_1806:
	v_max_f32_e32 v18, v84, v85
	v_max3_f32 v18, v18, v86, v87
	v_max3_f32 v18, v18, v88, v89
	v_max3_f32 v18, v18, v90, v91
	v_max3_f32 v18, v18, v92, v93
	v_max3_f32 v18, v18, v94, v95
	v_max3_f32 v18, v18, v96, v97
	v_max3_f32 v114, v18, v98, v99
	v_cmp_nle_f32_e32 vcc, v114, v226
	s_cbranch_vccnz .Lsel_resc_g0

; template <class G> __device__ __forceinline__ void online_sm8(f32x4 (&s)[4], G& g, const float ref) {
;     float mx = s[0][0];
; #pragma unroll
;     for (int T_ = 0; T_ < 4; ++T_)
; #pragma unroll
;         for (int i = 0; i < 4; ++i) mx = fmaxf(mx, s[T_][i]);
;     const float t = mx + (ref - 5.f);
;     if (!__all(t <= g.m + SM_THR8)) {
.LBB0_1812:
	v_max_f32_e32 v114, v84, v85
	v_max3_f32 v114, v114, v86, v87
	v_max3_f32 v114, v114, v88, v89
	v_max3_f32 v114, v114, v90, v91
	v_max3_f32 v114, v114, v92, v93
	v_max3_f32 v114, v114, v94, v95
	v_max3_f32 v114, v114, v96, v97
	v_max3_f32 v114, v114, v98, v99
	v_cmp_nle_f32_e32 vcc, v114, v227
	s_cbranch_vccnz .Lsel_resc_g1

; __device__ __forceinline__ float xmax16(float v) { float a = v, b = v; PL_SWAP16(a, b); return fmaxf(a, b); }
; __device__ __forceinline__ float xmax32(float v) { float a = v, b = v; PL_SWAP32(a, b); return fmaxf(a, b); }
; template <class G> __device__ __forceinline__ void online_sm8(f32x4 (&s)[4], G& g, const float ref) {
;     ...
;     if (!__all(t <= g.m + SM_THR8)) {
;         const float mr = xmax32(xmax16(t));
;         const float mn = fmaxf(g.m, mr); const float al = __builtin_amdgcn_exp2f(g.m - mn); g.m = mn; g.l *= al;
; #pragma unroll
;         for (int dt = 0; dt < 8; ++dt) g.o[dt] = g.o[dt] * al;
;         const float d = ref - mn;
; #pragma unroll
;         for (int T_ = 0; T_ < 4; ++T_)
; #pragma unroll
;             for (int i = 0; i < 4; ++i) s[T_][i] += d;
;     }
.Lsel_resc_g0:
	v_add_f32_e32 v150, v217, v114
	v_mov_b32_e32 v18, v84
	v_mov_b32_e32 v84, v150
	s_nop 1
	v_permlane16_swap_b32 v84, v150
	v_mov_b32_e32 v151, v96
	v_max_f32_e32 v114, v150, v150
	v_max_f32_e32 v84, v84, v84
	v_max_f32_e32 v84, v84, v114
	v_mov_b32_e32 v114, v84
	s_nop 1
	v_permlane32_swap_b32 v114, v84
	v_mov_b32_e32 v150, v92
	v_max3_f32 v114, v19, v114, v84
	v_sub_f32_e32 v19, v19, v114
	v_exp_f32_e32 v84, v19
	v_mov_b32_e32 v19, v88
	v_mov_b32_e32 v210, v85
	v_mov_b32_e32 v211, v86
	v_mul_f32_e32 v183, v183, v84
	v_pk_mul_f32 v[82:83], v[82:83], v[84:85] op_sel_hi:[1,0]
	v_pk_mul_f32 v[80:81], v[80:81], v[84:85] op_sel_hi:[1,0]
	v_pk_mul_f32 v[78:79], v[78:79], v[84:85] op_sel_hi:[1,0]
	v_pk_mul_f32 v[76:77], v[76:77], v[84:85] op_sel_hi:[1,0]
	v_pk_mul_f32 v[74:75], v[74:75], v[84:85] op_sel_hi:[1,0]
	v_pk_mul_f32 v[72:73], v[72:73], v[84:85] op_sel_hi:[1,0]
	v_pk_mul_f32 v[70:71], v[70:71], v[84:85] op_sel_hi:[1,0]
	v_pk_mul_f32 v[68:69], v[68:69], v[84:85] op_sel_hi:[1,0]
	v_pk_mul_f32 v[66:67], v[66:67], v[84:85] op_sel_hi:[1,0]
	v_pk_mul_f32 v[64:65], v[64:65], v[84:85] op_sel_hi:[1,0]
	v_pk_mul_f32 v[62:63], v[62:63], v[84:85] op_sel_hi:[1,0]
	v_pk_mul_f32 v[60:61], v[60:61], v[84:85] op_sel_hi:[1,0]
	v_pk_mul_f32 v[58:59], v[58:59], v[84:85] op_sel_hi:[1,0]
	v_pk_mul_f32 v[56:57], v[56:57], v[84:85] op_sel_hi:[1,0]
	v_pk_mul_f32 v[54:55], v[54:55], v[84:85] op_sel_hi:[1,0]
	v_pk_mul_f32 v[52:53], v[52:53], v[84:85] op_sel_hi:[1,0]
	v_sub_f32_e32 v84, v219, v114
	v_pk_add_f32 v[212:213], v[18:19], v[84:85] op_sel_hi:[1,0]
	v_mov_b32_e32 v18, v89
	v_mov_b32_e32 v19, v90
	v_pk_add_f32 v[214:215], v[18:19], v[84:85] op_sel_hi:[1,0]
	v_mov_b32_e32 v18, v93
	v_mov_b32_e32 v19, v94
	v_pk_add_f32 v[88:89], v[18:19], v[84:85] op_sel_hi:[1,0]
	v_mov_b32_e32 v18, v97
	v_mov_b32_e32 v19, v98
	v_pk_add_f32 v[210:211], v[210:211], v[84:85] op_sel_hi:[1,0]
	v_pk_add_f32 v[150:151], v[150:151], v[84:85] op_sel_hi:[1,0]
	v_pk_add_f32 v[92:93], v[18:19], v[84:85] op_sel_hi:[1,0]
	v_add_f32_e32 v87, v87, v84
	v_add_f32_e32 v91, v91, v84
	v_add_f32_e32 v95, v95, v84
	v_add_f32_e32 v99, v99, v84
	v_mov_b32_e32 v19, v114
	v_cmp_ngt_f32_e32 vcc, s90, v19
	v_mov_b32_e32 v97, v92
	v_mov_b32_e32 v98, v93
	v_mov_b32_e32 v93, v88
	v_mov_b32_e32 v94, v89
	v_mov_b32_e32 v89, v214
	v_mov_b32_e32 v90, v215
	v_mov_b32_e32 v85, v210
	v_mov_b32_e32 v86, v211
	v_mov_b32_e32 v84, v212
	v_mov_b32_e32 v88, v213
	v_mov_b32_e32 v92, v150
	v_mov_b32_e32 v96, v151
	v_cndmask_b32_e32 v219, 0, v19, vcc
	v_add_f32_e32 v218, v19, v115
	v_sub_f32_e32 v216, 0x40a00000, v219
	v_add_f32_e32 v217, 0xc0a00000, v219
	v_sub_f32_e32 v226, v218, v217
	s_branch .LBB0_1808

; __device__ __forceinline__ float xmax16(float v) { float a = v, b = v; PL_SWAP16(a, b); return fmaxf(a, b); }
; __device__ __forceinline__ float xmax32(float v) { float a = v, b = v; PL_SWAP32(a, b); return fmaxf(a, b); }
; template <class G> __device__ __forceinline__ void online_sm8(f32x4 (&s)[4], G& g, const float ref) {
;     ...
;     if (!__all(t <= g.m + SM_THR8)) {
;         const float mr = xmax32(xmax16(t));
;         const float mn = fmaxf(g.m, mr); const float al = __builtin_amdgcn_exp2f(g.m - mn); g.m = mn; g.l *= al;
; #pragma unroll
;         for (int dt = 0; dt < 8; ++dt) g.o[dt] = g.o[dt] * al;
;         const float d = ref - mn;
; #pragma unroll
;         for (int T_ = 0; T_ < 4; ++T_)
; #pragma unroll
;             for (int i = 0; i < 4; ++i) s[T_][i] += d;
;     }
.Lsel_resc_g1:
	v_add_f32_e32 v150, v221, v114
	v_mov_b32_e32 v116, v84
	v_mov_b32_e32 v84, v150
	s_nop 1
	v_permlane16_swap_b32 v150, v84
	v_mov_b32_e32 v151, v96
	v_max_f32_e32 v84, v84, v84
	v_max_f32_e32 v114, v150, v150
	v_max_f32_e32 v84, v114, v84
	v_mov_b32_e32 v114, v84
	s_nop 1
	v_permlane32_swap_b32 v84, v114
	v_mov_b32_e32 v150, v92
	v_max3_f32 v114, v117, v84, v114
	v_sub_f32_e32 v84, v117, v114
	v_exp_f32_e32 v84, v84
	v_sub_f32_e32 v18, v223, v114
	v_mov_b32_e32 v117, v88
	v_mov_b32_e32 v88, v93
	v_mul_f32_e32 v182, v182, v84
	v_pk_mul_f32 v[50:51], v[50:51], v[84:85] op_sel_hi:[1,0]
	v_pk_mul_f32 v[48:49], v[48:49], v[84:85] op_sel_hi:[1,0]
	v_pk_mul_f32 v[46:47], v[46:47], v[84:85] op_sel_hi:[1,0]
	v_pk_mul_f32 v[44:45], v[44:45], v[84:85] op_sel_hi:[1,0]
	v_pk_mul_f32 v[42:43], v[42:43], v[84:85] op_sel_hi:[1,0]
	v_pk_mul_f32 v[40:41], v[40:41], v[84:85] op_sel_hi:[1,0]
	v_pk_mul_f32 v[38:39], v[38:39], v[84:85] op_sel_hi:[1,0]
	v_pk_mul_f32 v[36:37], v[36:37], v[84:85] op_sel_hi:[1,0]
	v_pk_mul_f32 v[34:35], v[34:35], v[84:85] op_sel_hi:[1,0]
	v_pk_mul_f32 v[32:33], v[32:33], v[84:85] op_sel_hi:[1,0]
	v_pk_mul_f32 v[30:31], v[30:31], v[84:85] op_sel_hi:[1,0]
	v_pk_mul_f32 v[28:29], v[28:29], v[84:85] op_sel_hi:[1,0]
	v_pk_mul_f32 v[26:27], v[26:27], v[84:85] op_sel_hi:[1,0]
	v_pk_mul_f32 v[24:25], v[24:25], v[84:85] op_sel_hi:[1,0]
	v_pk_mul_f32 v[22:23], v[22:23], v[84:85] op_sel_hi:[1,0]
	v_pk_mul_f32 v[20:21], v[20:21], v[84:85] op_sel_hi:[1,0]
	v_mov_b32_e32 v84, v85
	v_mov_b32_e32 v85, v86
	v_pk_add_f32 v[210:211], v[84:85], v[18:19] op_sel_hi:[1,0]
	v_mov_b32_e32 v84, v89
	v_mov_b32_e32 v85, v90
	v_mov_b32_e32 v89, v94
	v_mov_b32_e32 v92, v97
	v_mov_b32_e32 v93, v98
	v_pk_add_f32 v[212:213], v[116:117], v[18:19] op_sel_hi:[1,0]
	v_pk_add_f32 v[84:85], v[84:85], v[18:19] op_sel_hi:[1,0]
	v_pk_add_f32 v[88:89], v[88:89], v[18:19] op_sel_hi:[1,0]
	v_pk_add_f32 v[150:151], v[150:151], v[18:19] op_sel_hi:[1,0]
	v_pk_add_f32 v[92:93], v[92:93], v[18:19] op_sel_hi:[1,0]
	v_add_f32_e32 v87, v87, v18
	v_add_f32_e32 v91, v91, v18
	v_add_f32_e32 v95, v95, v18
	v_add_f32_e32 v99, v99, v18
	v_mov_b32_e32 v117, v114
	v_cmp_ngt_f32_e32 vcc, s90, v117
	v_mov_b32_e32 v97, v92
	v_mov_b32_e32 v98, v93
	v_mov_b32_e32 v93, v88
	v_mov_b32_e32 v94, v89
	v_mov_b32_e32 v89, v84
	v_mov_b32_e32 v90, v85
	v_mov_b32_e32 v85, v210
	v_mov_b32_e32 v86, v211
	v_mov_b32_e32 v84, v212
	v_mov_b32_e32 v88, v213
	v_mov_b32_e32 v92, v150
	v_mov_b32_e32 v96, v151
	v_cndmask_b32_e32 v223, 0, v117, vcc
	v_add_f32_e32 v222, v117, v115
	v_sub_f32_e32 v220, 0x40a00000, v223
	v_add_f32_e32 v221, 0xc0a00000, v223
	v_sub_f32_e32 v227, v222, v221
	s_branch .LBB0_1797
